# SWA unit K staging: 4 (2) row-group loads issued together with one wait; T1 counted wait vmcnt(16)
# speedup vs baseline: 1.0086x; 1.0009x over previous
; #define LAS __attribute__((address_space(3)))
; __device__ __forceinline__ void stage_kv(LAS unsigned char* lds, const bf16_t* kcol, const bf16_t* vcol, size_t grow0, int nk, int kc0, int tid) {
;     for (int c = tid; c < nk * 8; c += NTHR) { const int key = c >> 3, part = c & 7;
;         const u32x4 v = *(const u32x4*)(kcol + (grow0 + key) * NIN + part * 8);
;         *(LAS u32x4*)(lds + K_OFF + (kc0 + key) * KROW + part * 16) = v; }
.LBB0_895:
	v_lshl_add_u64 v[180:181], v[4:5], 0, s[42:43]
	v_lshl_add_u64 v[182:183], v[180:181], 0, s[42:43]
	v_lshl_add_u64 v[184:185], v[182:183], 0, s[42:43]
	global_load_dwordx4 v[164:167], v[4:5], off
	global_load_dwordx4 v[168:171], v[180:181], off
	global_load_dwordx4 v[172:175], v[182:183], off
	global_load_dwordx4 v[176:179], v[184:185], off
	s_waitcnt vmcnt(0)
	ds_write_b128 v6, v[164:167]
	ds_write_b128 v6, v[168:171] offset:9216
	ds_write_b128 v6, v[172:175] offset:18432
	ds_write_b128 v6, v[176:179] offset:27648
	v_lshl_add_u64 v[4:5], v[134:135], 0, s[12:13]
	s_mov_b64 s[12:13], 0
	v_mov_b32_e32 v3, v148
	v_mov_b32_e32 v6, v149

; #define LAS __attribute__((address_space(3)))
; __device__ __forceinline__ void stage_kv(LAS unsigned char* lds, const bf16_t* kcol, const bf16_t* vcol, size_t grow0, int nk, int kc0, int tid) {
;     for (int c = tid; c < nk * 8; c += NTHR) { const int key = c >> 3, part = c & 7;
;         const u32x4 v = *(const u32x4*)(kcol + (grow0 + key) * NIN + part * 8);
;         *(LAS u32x4*)(lds + K_OFF + (kc0 + key) * KROW + part * 16) = v; }
;     const int np = nk >> 1;
;     for (int it = tid; it < np * 8; it += NTHR) { const int kp = it % np, dp = it / np;
;         const u32x4 a = *(const u32x4*)(vcol + (grow0 + 2 * kp) * NIN + dp * 8), b = *(const u32x4*)(vcol + (grow0 + 2 * kp + 1) * NIN + dp * 8);
;         LAS unsigned char* dst = lds + V_OFF + (dp * 8) * VROW + (kc0 + 2 * kp) * 2;
;         *(LAS unsigned*)(dst + 0 * VROW) = (a.x & 0xffffu) | (b.x << 16); *(LAS unsigned*)(dst + 1 * VROW) = (a.x >> 16) | (b.x & 0xffff0000u);
;         *(LAS unsigned*)(dst + 2 * VROW) = (a.y & 0xffffu) | (b.y << 16); *(LAS unsigned*)(dst + 3 * VROW) = (a.y >> 16) | (b.y & 0xffff0000u);
;         *(LAS unsigned*)(dst + 4 * VROW) = (a.z & 0xffffu) | (b.z << 16); *(LAS unsigned*)(dst + 5 * VROW) = (a.z >> 16) | (b.z & 0xffff0000u);
;         *(LAS unsigned*)(dst + 6 * VROW) = (a.w & 0xffffu) | (b.w << 16); *(LAS unsigned*)(dst + 7 * VROW) = (a.w >> 16) | (b.w & 0xffff0000u); }
.LBB0_901:
	v_lshl_add_u64 v[180:181], v[4:5], 0, s[42:43]
	global_load_dwordx4 v[164:167], v[4:5], off
	global_load_dwordx4 v[168:171], v[180:181], off
	s_waitcnt vmcnt(0)
	ds_write_b128 v6, v[164:167]
	ds_write_b128 v6, v[168:171] offset:9216
	s_and_saveexec_b64 s[8:9], s[6:7]
	s_cbranch_execz .LBB0_904
	s_add_u32 s10, s3, s0
	s_addc_u32 s11, s4, 0
	v_or_b32_e32 v3, s46, v130
	v_mov_b64_e32 v[4:5], s[10:11]
	v_mad_u64_u32 v[4:5], s[10:11], v3, s54, v[4:5]
	v_mad_i32_i24 v5, s47, v152, v5
	v_mov_b32_e32 v139, v2
	v_lshl_add_u64 v[8:9], v[4:5], 0, v[138:139]
	s_movk_i32 s0, 0x2000
	global_load_dwordx4 v[4:7], v[8:9], off
	v_add_co_u32_e32 v8, vcc, s0, v8
	v_add_u32_e32 v3, 0x9000, v151
	s_nop 0
	v_addc_co_u32_e32 v9, vcc, 0, v9, vcc
	global_load_dwordx4 v[8:11], v[8:9], off offset:1536
	v_add_u32_e32 v12, 0x9400, v151
	v_add_u32_e32 v13, 0x9800, v151
	v_add_u32_e32 v14, 0x9c00, v151
	s_waitcnt vmcnt(1)
	v_and_b32_e32 v15, 0xffff, v4
	v_lshrrev_b32_e32 v4, 16, v4
	v_and_b32_e32 v16, 0xffff, v5
	v_lshrrev_b32_e32 v5, 16, v5
	v_and_b32_e32 v17, 0xffff, v6
	v_lshrrev_b32_e32 v6, 16, v6
	v_and_b32_e32 v19, 0xffff, v7
	v_lshrrev_b32_e32 v7, 16, v7
	s_waitcnt vmcnt(0)
	v_lshl_or_b32 v15, v8, 16, v15
	v_and_or_b32 v4, v8, s57, v4
	v_lshl_or_b32 v8, v9, 16, v16
	v_and_or_b32 v5, v9, s57, v5
	v_lshl_or_b32 v9, v10, 16, v17
	v_and_or_b32 v6, v10, s57, v6
	v_lshl_or_b32 v10, v11, 16, v19
	v_and_or_b32 v7, v11, s57, v7
	ds_write2_b32 v3, v15, v4 offset0:64 offset1:194
	ds_write2_b32 v12, v8, v5 offset0:68 offset1:198
	ds_write2_b32 v13, v9, v6 offset0:72 offset1:202
	ds_write2_b32 v14, v10, v7 offset0:76 offset1:206

; __device__ __forceinline__ float wave_max(float v) { return lane63(scan64<true>(v)); }
; template <int YMODE, int EXTRA, bool NORM_OUT, bool XN8  , bool XIN_BF = false  , bool XOUT_BF = false  > ...
;     ...
;                 if (XN8) {
;                     float am = 0.f;
; #pragma unroll
;                     for (int j = 0; j < 8; ++j) am = fmaxf(fmaxf(am, fmaxf(fabsf(x[j][0]), fabsf(x[j][1]))), fmaxf(fabsf(x[j][2]), fabsf(x[j][3])));
;                     am = wave_max(am);
;                     const float inv = am > 0.f ? 127.f / am : 0.f;
;                     if (F.lane == 0) { rowmax[row] = am; if (EXTRA == 2) route[384 + rl] = am; }
; #pragma unroll
;                     for (int j = 0; j < 8; ++j) *(unsigned*)((unsigned char*)XN + row * D + 256 * j + 4 * F.lane) = pack_i8x4(x[j][0] * inv, x[j][1] * inv, x[j][2] * inv, x[j][3] * inv);
.LBB0_1084:
	s_or_b64 exec, exec, s[8:9]
	v_div_scale_f32 v104, s[8:9], s14, s14, v125
	v_rcp_f32_e32 v105, v104
	v_mov_b32_e32 v106, s14
	v_div_scale_f32 v106, vcc, s21, v106, s21
	v_fma_f32 v107, -v104, v105, 1.0
	v_fmac_f32_e32 v105, v107, v105
	v_mul_f32_e32 v107, v106, v105
	v_fma_f32 v108, -v104, v107, v106
	v_fmac_f32_e32 v107, v108, v105
	v_fma_f32 v104, -v104, v107, v106
	v_div_fmas_f32 v104, v104, v105, v107
	v_div_fixup_f32 v104, v104, s14, v125
	v_cmp_gt_f32_e64 vcc, s14, 0
	s_lshl_b64 s[8:9], s[16:17], 11
	s_add_i32 s24, s24, 1
	v_cndmask_b32_e32 v104, 0, v104, vcc
	v_mul_f32_e32 v65, v65, v104
	v_mul_f32_e32 v61, v61, v104
	v_mul_f32_e32 v57, v57, v104
	v_mul_f32_e32 v53, v53, v104
	v_mul_f32_e32 v49, v49, v104
	v_mul_f32_e32 v45, v45, v104
	v_mul_f32_e32 v41, v41, v104
	v_mul_f32_e32 v37, v37, v104
	v_mul_f32_e32 v64, v64, v104
	v_mul_f32_e32 v62, v62, v104
	v_mul_f32_e32 v63, v63, v104
	v_med3_f32 v65, v65, s22, v125
	v_mul_f32_e32 v60, v60, v104
	v_mul_f32_e32 v58, v58, v104
	v_mul_f32_e32 v59, v59, v104
	v_med3_f32 v61, v61, s22, v125
	v_mul_f32_e32 v56, v56, v104
	v_mul_f32_e32 v54, v54, v104
	v_mul_f32_e32 v55, v55, v104
	v_med3_f32 v57, v57, s22, v125
	v_mul_f32_e32 v52, v52, v104
	v_mul_f32_e32 v50, v50, v104
	v_mul_f32_e32 v51, v51, v104
	v_med3_f32 v53, v53, s22, v125
	v_mul_f32_e32 v48, v48, v104
	v_mul_f32_e32 v46, v46, v104
	v_mul_f32_e32 v47, v47, v104
	v_med3_f32 v49, v49, s22, v125
	v_mul_f32_e32 v44, v44, v104
	v_mul_f32_e32 v42, v42, v104
	v_mul_f32_e32 v43, v43, v104
	v_med3_f32 v45, v45, s22, v125
	v_mul_f32_e32 v40, v40, v104
	v_mul_f32_e32 v38, v38, v104
	v_mul_f32_e32 v39, v39, v104
	v_med3_f32 v41, v41, s22, v125
	v_mul_f32_e32 v36, v36, v104
	v_mul_f32_e32 v34, v34, v104
	v_mul_f32_e32 v35, v35, v104
	v_med3_f32 v37, v37, s22, v125
	v_med3_f32 v64, v64, s22, v125
	v_rndne_f32_e32 v65, v65
	v_med3_f32 v62, v62, s22, v125
	v_med3_f32 v63, v63, s22, v125
	v_med3_f32 v60, v60, s22, v125
	v_rndne_f32_e32 v61, v61
	v_med3_f32 v58, v58, s22, v125
	v_med3_f32 v59, v59, s22, v125
	v_med3_f32 v56, v56, s22, v125
	v_rndne_f32_e32 v57, v57
	v_med3_f32 v54, v54, s22, v125
	v_med3_f32 v55, v55, s22, v125
	v_med3_f32 v52, v52, s22, v125
	v_rndne_f32_e32 v53, v53
	v_med3_f32 v50, v50, s22, v125
	v_med3_f32 v51, v51, s22, v125
	v_med3_f32 v48, v48, s22, v125
	v_rndne_f32_e32 v49, v49
	v_med3_f32 v46, v46, s22, v125
	v_med3_f32 v47, v47, s22, v125
	v_med3_f32 v44, v44, s22, v125
	v_rndne_f32_e32 v45, v45
	v_med3_f32 v42, v42, s22, v125
	v_med3_f32 v43, v43, s22, v125
	v_med3_f32 v40, v40, s22, v125
	v_rndne_f32_e32 v41, v41
	v_med3_f32 v38, v38, s22, v125
	v_med3_f32 v39, v39, s22, v125
	v_med3_f32 v36, v36, s22, v125
	v_rndne_f32_e32 v37, v37
	v_med3_f32 v34, v34, s22, v125
	v_med3_f32 v35, v35, s22, v125
	v_rndne_f32_e32 v64, v64
	v_cvt_i32_f32_e32 v65, v65
	v_rndne_f32_e32 v62, v62
	v_rndne_f32_e32 v63, v63
	v_rndne_f32_e32 v60, v60
	v_cvt_i32_f32_e32 v61, v61
	v_rndne_f32_e32 v58, v58
	v_rndne_f32_e32 v59, v59
	v_rndne_f32_e32 v56, v56
	v_cvt_i32_f32_e32 v57, v57
	v_rndne_f32_e32 v54, v54
	v_rndne_f32_e32 v55, v55
	v_rndne_f32_e32 v52, v52
	v_cvt_i32_f32_e32 v53, v53
	v_rndne_f32_e32 v50, v50
	v_rndne_f32_e32 v51, v51
	v_rndne_f32_e32 v48, v48
	v_cvt_i32_f32_e32 v49, v49
	v_rndne_f32_e32 v46, v46
	v_rndne_f32_e32 v47, v47
	v_rndne_f32_e32 v44, v44
	v_cvt_i32_f32_e32 v45, v45
	v_rndne_f32_e32 v42, v42
	v_rndne_f32_e32 v43, v43
	v_rndne_f32_e32 v40, v40
	v_cvt_i32_f32_e32 v41, v41
	v_rndne_f32_e32 v38, v38
	v_rndne_f32_e32 v39, v39
	v_rndne_f32_e32 v36, v36
	v_cvt_i32_f32_e32 v37, v37
	v_rndne_f32_e32 v34, v34
	v_rndne_f32_e32 v35, v35
	v_cvt_i32_f32_e32 v64, v64
	v_cvt_i32_f32_sdwa v62, v62 dst_sel:WORD_1 dst_unused:UNUSED_PAD src0_sel:DWORD
	v_cvt_i32_f32_e32 v63, v63
	v_cvt_i32_f32_e32 v60, v60
	v_cvt_i32_f32_sdwa v58, v58 dst_sel:WORD_1 dst_unused:UNUSED_PAD src0_sel:DWORD
	v_cvt_i32_f32_e32 v59, v59
	v_cvt_i32_f32_e32 v56, v56
	v_cvt_i32_f32_sdwa v54, v54 dst_sel:WORD_1 dst_unused:UNUSED_PAD src0_sel:DWORD
	v_cvt_i32_f32_e32 v55, v55
	v_cvt_i32_f32_e32 v52, v52
	v_cvt_i32_f32_sdwa v50, v50 dst_sel:WORD_1 dst_unused:UNUSED_PAD src0_sel:DWORD
	v_cvt_i32_f32_e32 v51, v51
	v_cvt_i32_f32_e32 v48, v48
	v_cvt_i32_f32_sdwa v46, v46 dst_sel:WORD_1 dst_unused:UNUSED_PAD src0_sel:DWORD
	v_cvt_i32_f32_e32 v47, v47
	v_cvt_i32_f32_e32 v44, v44
	v_cvt_i32_f32_sdwa v42, v42 dst_sel:WORD_1 dst_unused:UNUSED_PAD src0_sel:DWORD
	v_cvt_i32_f32_e32 v43, v43
	v_cvt_i32_f32_e32 v40, v40
	v_cvt_i32_f32_sdwa v38, v38 dst_sel:WORD_1 dst_unused:UNUSED_PAD src0_sel:DWORD
	v_cvt_i32_f32_e32 v39, v39
	v_cvt_i32_f32_e32 v36, v36
	v_cvt_i32_f32_sdwa v34, v34 dst_sel:WORD_1 dst_unused:UNUSED_PAD src0_sel:DWORD
	v_cvt_i32_f32_e32 v35, v35
	v_lshlrev_b32_e32 v65, 8, v65
	v_lshlrev_b32_e32 v61, 8, v61
	v_lshlrev_b32_e32 v57, 8, v57
	v_lshlrev_b32_e32 v53, 8, v53
	v_lshlrev_b32_e32 v49, 8, v49
	v_lshlrev_b32_e32 v45, 8, v45
	v_lshlrev_b32_e32 v41, 8, v41
	v_lshlrev_b32_e32 v37, 8, v37
	v_and_b32_e32 v65, 0xff00, v65
	v_and_b32_e32 v62, 0xff0000, v62
	v_perm_b32 v63, v63, v64, s23
	v_and_b32_e32 v61, 0xff00, v61
	v_and_b32_e32 v58, 0xff0000, v58
	v_perm_b32 v59, v59, v60, s23
	v_and_b32_e32 v57, 0xff00, v57
	v_and_b32_e32 v54, 0xff0000, v54
	v_perm_b32 v55, v55, v56, s23
	v_and_b32_e32 v53, 0xff00, v53
	v_and_b32_e32 v50, 0xff0000, v50
	v_perm_b32 v51, v51, v52, s23
	v_and_b32_e32 v49, 0xff00, v49
	v_and_b32_e32 v46, 0xff0000, v46
	v_perm_b32 v47, v47, v48, s23
	v_and_b32_e32 v45, 0xff00, v45
	v_and_b32_e32 v42, 0xff0000, v42
	v_perm_b32 v43, v43, v44, s23
	v_and_b32_e32 v41, 0xff00, v41
	v_and_b32_e32 v38, 0xff0000, v38
	v_perm_b32 v39, v39, v40, s23
	v_and_b32_e32 v37, 0xff00, v37
	v_and_b32_e32 v34, 0xff0000, v34
	v_perm_b32 v35, v35, v36, s23
	v_or3_b32 v64, v63, v65, v62
	v_lshl_add_u64 v[62:63], v[86:87], 0, s[8:9]
	v_or3_b32 v58, v59, v61, v58
	v_or3_b32 v54, v55, v57, v54
	v_or3_b32 v50, v51, v53, v50
	v_or3_b32 v46, v47, v49, v46
	v_or3_b32 v42, v43, v45, v42
	v_or3_b32 v38, v39, v41, v38
	v_or3_b32 v34, v35, v37, v34
	global_store_dword v[62:63], v64, off
	global_store_dword v[62:63], v58, off offset:256
	global_store_dword v[62:63], v54, off offset:512
	global_store_dword v[62:63], v50, off offset:768
	global_store_dword v[62:63], v46, off offset:1024
	global_store_dword v[62:63], v42, off offset:1280
	global_store_dword v[62:63], v38, off offset:1536
	global_store_dword v[62:63], v34, off offset:1792
	s_waitcnt vmcnt(16)
; __device__ __forceinline__ float bflo(unsigned u) { return __uint_as_float(u << 16); }
; __device__ __forceinline__ float bfhi(unsigned u) { return __uint_as_float(u & 0xffff0000u); }
; template <int YMODE, int EXTRA, bool NORM_OUT, bool XN8  , bool XIN_BF = false  , bool XOUT_BF = false  > ...
;     ...
;         RP_LOAD(0);
; #pragma unroll 1
;         for (int rr = 0; rr < 8; ++rr) {
;             const int rl = F.wave * 8 + ((rr + blk) & 7); const size_t row = (size_t)blk * 64 + rl;
;             asm volatile("" ::: "memory");
;             f32x4 x[8];
; #pragma unroll
;             for (int j = 0; j < 8; ++j) x[j] = XIN_BF ? (f32x4){bflo(xrb[j].x), bfhi(xrb[j].x), bflo(xrb[j].y), bfhi(xrb[j].y)} : xr[j];
;             f32x4 y[8];
;             if (YMODE == 1) {
; #pragma unroll
;                 for (int j = 0; j < 8; ++j) y[j] = (f32x4){bflo(yr[j].x), bfhi(yr[j].x), bflo(yr[j].y), bfhi(yr[j].y)};
;             }
;             if (YMODE == 2) {
; #pragma unroll
;                 for (int j = 0; j < 8; ++j) y[j] = (f32x4){bflo(yr[j].x), bfhi(yr[j].x), bflo(yr[j].y), bfhi(yr[j].y)} * w1n + (f32x4){bflo(yr2[j].x), bfhi(yr2[j].x), bflo(yr2[j].y), bfhi(yr2[j].y)} * w2n;
;             }
;             if (rr < 7) RP_LOAD(rr + 1);
	v_mov_b64_e32 v[64:65], v[4:5]
	v_mov_b64_e32 v[60:61], v[8:9]
	v_mov_b64_e32 v[56:57], v[12:13]
	v_mov_b64_e32 v[52:53], v[16:17]
	v_mov_b64_e32 v[48:49], v[20:21]
	v_mov_b64_e32 v[44:45], v[24:25]
	v_mov_b64_e32 v[40:41], v[28:29]
	v_mov_b64_e32 v[36:37], v[32:33]
	s_cmp_eq_u32 s24, 8
	v_mov_b64_e32 v[104:105], v[88:89]
	v_mov_b64_e32 v[106:107], v[90:91]
	v_mov_b64_e32 v[108:109], v[92:93]
	v_mov_b64_e32 v[110:111], v[94:95]
	v_mov_b64_e32 v[112:113], v[96:97]
	v_mov_b64_e32 v[114:115], v[98:99]
	v_mov_b64_e32 v[116:117], v[100:101]
	v_mov_b64_e32 v[118:119], v[102:103]
	v_mov_b64_e32 v[62:63], v[2:3]
	v_mov_b64_e32 v[58:59], v[6:7]
	v_mov_b64_e32 v[54:55], v[10:11]
	v_mov_b64_e32 v[50:51], v[14:15]
	v_mov_b64_e32 v[46:47], v[18:19]
	v_mov_b64_e32 v[42:43], v[22:23]
	v_mov_b64_e32 v[38:39], v[26:27]
	v_mov_b64_e32 v[34:35], v[30:31]
	s_cbranch_scc1 .LBB0_1082

; #define LAS __attribute__((address_space(3)))
; __device__ __forceinline__ void stage_kv(LAS unsigned char* lds, const bf16_t* kcol, const bf16_t* vcol, size_t grow0, int nk, int kc0, int tid) {
;     for (int c = tid; c < nk * 8; c += NTHR) { const int key = c >> 3, part = c & 7;
;         const u32x4 v = *(const u32x4*)(kcol + (grow0 + key) * NIN + part * 8);
;         *(LAS u32x4*)(lds + K_OFF + (kc0 + key) * KROW + part * 16) = v; }
.LBB0_2004:
	v_lshl_add_u64 v[180:181], v[4:5], 0, s[42:43]
	v_lshl_add_u64 v[182:183], v[180:181], 0, s[42:43]
	v_lshl_add_u64 v[184:185], v[182:183], 0, s[42:43]
	global_load_dwordx4 v[164:167], v[4:5], off
	global_load_dwordx4 v[168:171], v[180:181], off
	global_load_dwordx4 v[172:175], v[182:183], off
	global_load_dwordx4 v[176:179], v[184:185], off
	s_waitcnt vmcnt(0)
	ds_write_b128 v7, v[164:167]
	ds_write_b128 v7, v[168:171] offset:9216
	ds_write_b128 v7, v[172:175] offset:18432
	ds_write_b128 v7, v[176:179] offset:27648
	v_lshl_add_u64 v[4:5], v[134:135], 0, s[12:13]
	s_mov_b64 s[12:13], 0
	v_mov_b32_e32 v6, v143
	v_mov_b32_e32 v7, v148

; #define LAS __attribute__((address_space(3)))
; __device__ __forceinline__ void stage_kv(LAS unsigned char* lds, const bf16_t* kcol, const bf16_t* vcol, size_t grow0, int nk, int kc0, int tid) {
;     for (int c = tid; c < nk * 8; c += NTHR) { const int key = c >> 3, part = c & 7;
;         const u32x4 v = *(const u32x4*)(kcol + (grow0 + key) * NIN + part * 8);
;         *(LAS u32x4*)(lds + K_OFF + (kc0 + key) * KROW + part * 16) = v; }
;     const int np = nk >> 1;
;     for (int it = tid; it < np * 8; it += NTHR) { const int kp = it % np, dp = it / np;
;         const u32x4 a = *(const u32x4*)(vcol + (grow0 + 2 * kp) * NIN + dp * 8), b = *(const u32x4*)(vcol + (grow0 + 2 * kp + 1) * NIN + dp * 8);
;         LAS unsigned char* dst = lds + V_OFF + (dp * 8) * VROW + (kc0 + 2 * kp) * 2;
;         *(LAS unsigned*)(dst + 0 * VROW) = (a.x & 0xffffu) | (b.x << 16); *(LAS unsigned*)(dst + 1 * VROW) = (a.x >> 16) | (b.x & 0xffff0000u);
;         *(LAS unsigned*)(dst + 2 * VROW) = (a.y & 0xffffu) | (b.y << 16); *(LAS unsigned*)(dst + 3 * VROW) = (a.y >> 16) | (b.y & 0xffff0000u);
;         *(LAS unsigned*)(dst + 4 * VROW) = (a.z & 0xffffu) | (b.z << 16); *(LAS unsigned*)(dst + 5 * VROW) = (a.z >> 16) | (b.z & 0xffff0000u);
;         *(LAS unsigned*)(dst + 6 * VROW) = (a.w & 0xffffu) | (b.w << 16); *(LAS unsigned*)(dst + 7 * VROW) = (a.w >> 16) | (b.w & 0xffff0000u); }
.LBB0_2010:
	v_lshl_add_u64 v[180:181], v[4:5], 0, s[42:43]
	global_load_dwordx4 v[164:167], v[4:5], off
	global_load_dwordx4 v[168:171], v[180:181], off
	s_waitcnt vmcnt(0)
	ds_write_b128 v7, v[164:167]
	ds_write_b128 v7, v[168:171] offset:9216
	s_and_saveexec_b64 s[8:9], s[6:7]
	s_cbranch_execz .LBB0_2013
	s_add_u32 s10, s3, s0
	s_addc_u32 s11, s4, 0
	v_or_b32_e32 v6, s54, v130
	v_mov_b64_e32 v[4:5], s[10:11]
	v_mad_u64_u32 v[4:5], s[10:11], v6, s56, v[4:5]
	v_mad_i32_i24 v5, s55, v151, v5
	v_mov_b32_e32 v139, v2
	v_lshl_add_u64 v[8:9], v[4:5], 0, v[138:139]
	global_load_dwordx4 v[4:7], v[8:9], off
	v_add_co_u32_e32 v8, vcc, s64, v8
	v_add_u32_e32 v12, 0x9000, v150
	s_nop 0
	v_addc_co_u32_e32 v9, vcc, 0, v9, vcc
	global_load_dwordx4 v[8:11], v[8:9], off offset:1536
	v_add_u32_e32 v13, 0x9400, v150
	v_add_u32_e32 v14, 0x9800, v150
	v_add_u32_e32 v15, 0x9c00, v150
	s_waitcnt vmcnt(1)
	v_and_b32_e32 v16, 0xffff, v4
	v_lshrrev_b32_e32 v4, 16, v4
	v_and_b32_e32 v17, 0xffff, v5
	v_lshrrev_b32_e32 v5, 16, v5
	v_and_b32_e32 v19, 0xffff, v6
	v_lshrrev_b32_e32 v6, 16, v6
	v_and_b32_e32 v20, 0xffff, v7
	v_lshrrev_b32_e32 v7, 16, v7
	s_waitcnt vmcnt(0)
	v_lshl_or_b32 v16, v8, 16, v16
	v_and_or_b32 v4, v8, s65, v4
	v_lshl_or_b32 v8, v9, 16, v17
	v_and_or_b32 v5, v9, s65, v5
	v_lshl_or_b32 v9, v10, 16, v19
	v_and_or_b32 v6, v10, s65, v6
	v_lshl_or_b32 v10, v11, 16, v20
	v_and_or_b32 v7, v11, s65, v7
	ds_write2_b32 v12, v16, v4 offset0:64 offset1:194
	ds_write2_b32 v13, v8, v5 offset0:68 offset1:198
	ds_write2_b32 v14, v9, v6 offset0:72 offset1:202
	ds_write2_b32 v15, v10, v7 offset0:76 offset1:206
